# tconv8 epilogue hand-written: permlane16_swap pairs widen the ZT/Z8 stores to dwordx4/dwordx2, operand loads double-buffered one 8-tile group ahead, group-level counted vmcnt, hardware bf16 convert
# speedup vs baseline: 1.0182x; 1.0033x over previous
.LBB0_539:
	s_add_i32 s5, s4, 0x80
	s_and_b32 s72, s5, 0xf80
	v_lshl_add_u64 v[168:169], v[188:189], 0, s[72:73]
	global_load_dwordx4 v[172:175], v[168:169], off
	s_nop 0
	global_load_dwordx4 v[168:171], v[168:169], off offset:16
	v_add_u32_e32 v185, s4, v192
	v_add_u32_e32 v203, s72, v192
	ds_read_b128 v[204:207], v185 offset:320
	ds_read_b128 v[208:211], v185 offset:336
	ds_read_b128 v[212:215], v185 offset:352
	ds_read_b128 v[216:219], v185 offset:368
	ds_read_b128 v[220:223], v185 offset:384
	ds_read_b128 v[224:227], v185 offset:400
	ds_read_b128 v[228:231], v185 offset:416
	s_waitcnt vmcnt(2) lgkmcnt(7)
	v_mfma_f32_16x16x128_f8f6f4 v[164:167], v[28:35], v[0:7], v[164:167]
	v_mfma_f32_16x16x128_f8f6f4 v[160:163], v[24:31], v[0:7], v[160:163]
	v_mfma_f32_16x16x128_f8f6f4 v[156:159], v[20:27], v[0:7], v[156:159]
	v_mfma_f32_16x16x128_f8f6f4 v[152:155], v[16:23], v[0:7], v[152:155]
	v_mfma_f32_16x16x128_f8f6f4 v[148:151], v[12:19], v[0:7], v[148:151]
	v_mfma_f32_16x16x128_f8f6f4 v[144:147], v[8:15], v[0:7], v[144:147]
	ds_read_b128 v[8:11], v185 offset:240
	ds_read_b128 v[12:15], v185 offset:256
	ds_read_b128 v[16:19], v185 offset:272
	ds_read_b128 v[20:23], v185 offset:288
	ds_read_b128 v[24:27], v185 offset:304
	ds_read_b128 v[28:31], v185 offset:320
	s_waitcnt lgkmcnt(6)
	v_mfma_f32_16x16x128_f8f6f4 v[140:143], v[224:231], v[0:7], v[140:143]
	v_mfma_f32_16x16x128_f8f6f4 v[136:139], v[220:227], v[0:7], v[136:139]
	v_mfma_f32_16x16x128_f8f6f4 v[132:135], v[216:223], v[0:7], v[132:135]
	v_mfma_f32_16x16x128_f8f6f4 v[128:131], v[212:219], v[0:7], v[128:131]
	v_mfma_f32_16x16x128_f8f6f4 v[124:127], v[208:215], v[0:7], v[124:127]
	v_mfma_f32_16x16x128_f8f6f4 v[120:123], v[204:211], v[0:7], v[120:123]
	ds_read_b128 v[204:207], v185 offset:160
	ds_read_b128 v[208:211], v185 offset:176
	ds_read_b128 v[212:215], v185 offset:192
	ds_read_b128 v[216:219], v185 offset:208
	ds_read_b128 v[220:223], v185 offset:224
	ds_read_b128 v[224:227], v185 offset:240
	s_waitcnt lgkmcnt(6)
	v_mfma_f32_16x16x128_f8f6f4 v[116:119], v[24:31], v[0:7], v[116:119]
	v_mfma_f32_16x16x128_f8f6f4 v[112:115], v[20:27], v[0:7], v[112:115]
	v_mfma_f32_16x16x128_f8f6f4 v[108:111], v[16:23], v[0:7], v[108:111]
	v_mfma_f32_16x16x128_f8f6f4 v[104:107], v[12:19], v[0:7], v[104:107]
	v_mfma_f32_16x16x128_f8f6f4 v[100:103], v[8:15], v[0:7], v[100:103]
	ds_read_b128 v[8:11], v185 offset:80
	ds_read_b128 v[12:15], v185 offset:96
	ds_read_b128 v[16:19], v185 offset:112
	ds_read_b128 v[20:23], v185 offset:128
	ds_read_b128 v[24:27], v185 offset:144
	ds_read_b128 v[28:31], v185 offset:160
	s_waitcnt lgkmcnt(6)
	v_mfma_f32_16x16x128_f8f6f4 v[96:99], v[220:227], v[0:7], v[96:99]
	v_mfma_f32_16x16x128_f8f6f4 v[92:95], v[216:223], v[0:7], v[92:95]
	v_mfma_f32_16x16x128_f8f6f4 v[88:91], v[212:219], v[0:7], v[88:91]
	v_mfma_f32_16x16x128_f8f6f4 v[84:87], v[208:215], v[0:7], v[84:87]
	v_mfma_f32_16x16x128_f8f6f4 v[80:83], v[204:211], v[0:7], v[80:83]
	ds_read_b128 v[204:207], v185 offset:0
	ds_read_b128 v[208:211], v185 offset:16
	ds_read_b128 v[212:215], v185 offset:32
	ds_read_b128 v[216:219], v185 offset:48
	ds_read_b128 v[220:223], v185 offset:64
	ds_read_b128 v[224:227], v185 offset:80
	s_waitcnt lgkmcnt(6)
	v_mfma_f32_16x16x128_f8f6f4 v[76:79], v[24:31], v[0:7], v[76:79]
	v_mfma_f32_16x16x128_f8f6f4 v[72:75], v[20:27], v[0:7], v[72:75]
	v_mfma_f32_16x16x128_f8f6f4 v[68:71], v[16:23], v[0:7], v[68:71]
	v_mfma_f32_16x16x128_f8f6f4 v[64:67], v[12:19], v[0:7], v[64:67]
	v_mfma_f32_16x16x128_f8f6f4 v[60:63], v[8:15], v[0:7], v[60:63]
	ds_read_b128 v[8:11], v203 offset:416
	ds_read_b128 v[12:15], v203 offset:432
	ds_read_b128 v[16:19], v203 offset:448
	ds_read_b128 v[20:23], v203 offset:464
	ds_read_b128 v[24:27], v203 offset:480
	ds_read_b128 v[28:31], v203 offset:496
	ds_read_b128 v[32:35], v203 offset:512
	s_waitcnt lgkmcnt(7)
	v_mfma_f32_16x16x128_f8f6f4 v[56:59], v[220:227], v[0:7], v[56:59]
	v_mfma_f32_16x16x128_f8f6f4 v[52:55], v[216:223], v[0:7], v[52:55]
	v_mfma_f32_16x16x128_f8f6f4 v[48:51], v[212:219], v[0:7], v[48:51]
	v_mfma_f32_16x16x128_f8f6f4 v[44:47], v[208:215], v[0:7], v[44:47]
	v_mfma_f32_16x16x128_f8f6f4 v[40:43], v[204:211], v[0:7], v[40:43]
	s_cmpk_eq_i32 s5, 0x1000
	s_mov_b32 s4, s5
	s_waitcnt vmcnt(0)
	v_mov_b32_e32 v0, v172
	v_mov_b32_e32 v1, v173
	v_mov_b32_e32 v2, v174
	v_mov_b32_e32 v3, v175
	v_mov_b32_e32 v4, v168
	v_mov_b32_e32 v5, v169
	v_mov_b32_e32 v6, v170
	v_mov_b32_e32 v7, v171
	s_cbranch_scc0 .LBB0_539
	s_waitcnt lgkmcnt(0)
	s_lshl_b64 s[4:5], s[36:37], 2
	s_add_u32 s4, s31, s4
	s_addc_u32 s5, s46, s5
	global_load_dword v4, v245, s[4:5]
	v_lshl_add_u64 v[0:1], v[186:187], 0, v[182:183]
	v_lshlrev_b64 v[2:3], 1, v[0:1]
	v_lshl_add_u64 v[8:9], s[22:23], 0, v[2:3]
	v_lshl_add_u64 v[6:7], s[24:25], 0, v[2:3]
	global_load_dwordx2 v[204:205], v[8:9], off
	global_load_dwordx2 v[206:207], v[6:7], off
	global_load_dwordx2 v[208:209], v[8:9], off offset:32
	global_load_dwordx2 v[210:211], v[6:7], off offset:32
	global_load_dwordx2 v[212:213], v[8:9], off offset:64
	global_load_dwordx2 v[214:215], v[6:7], off offset:64
	global_load_dwordx2 v[216:217], v[8:9], off offset:96
	global_load_dwordx2 v[218:219], v[6:7], off offset:96
	global_load_dwordx2 v[220:221], v[8:9], off offset:128
	global_load_dwordx2 v[222:223], v[6:7], off offset:128
	global_load_dwordx2 v[224:225], v[8:9], off offset:160
	global_load_dwordx2 v[226:227], v[6:7], off offset:160
	global_load_dwordx2 v[228:229], v[8:9], off offset:192
	global_load_dwordx2 v[230:231], v[6:7], off offset:192
	global_load_dwordx2 v[232:233], v[8:9], off offset:224
	global_load_dwordx2 v[234:235], v[6:7], off offset:224
	s_waitcnt lgkmcnt(0)
	global_load_dwordx2 v[10:11], v[8:9], off offset:256
	global_load_dwordx2 v[12:13], v[6:7], off offset:256
	global_load_dwordx2 v[14:15], v[8:9], off offset:288
	global_load_dwordx2 v[16:17], v[6:7], off offset:288
	global_load_dwordx2 v[18:19], v[8:9], off offset:320
	global_load_dwordx2 v[20:21], v[6:7], off offset:320
	global_load_dwordx2 v[22:23], v[8:9], off offset:352
	global_load_dwordx2 v[24:25], v[6:7], off offset:352
	global_load_dwordx2 v[26:27], v[8:9], off offset:384
	global_load_dwordx2 v[28:29], v[6:7], off offset:384
	global_load_dwordx2 v[30:31], v[8:9], off offset:416
	global_load_dwordx2 v[32:33], v[6:7], off offset:416
	global_load_dwordx2 v[34:35], v[8:9], off offset:448
	global_load_dwordx2 v[36:37], v[6:7], off offset:448
	global_load_dwordx2 v[236:237], v[8:9], off offset:480
	global_load_dwordx2 v[238:239], v[6:7], off offset:480
	v_lshl_add_u64 v[2:3], s[26:27], 0, v[2:3]
	v_lshl_add_u64 v[0:1], s[28:29], 0, v[0:1]
	v_mbcnt_lo_u32_b32 v5, -1, 0
	v_mbcnt_hi_u32_b32 v5, -1, v5
	v_and_b32_e32 v5, 16, v5
	v_lshrrev_b32_e32 v38, 1, v5
	v_add_u32_e32 v39, v5, v38
	v_lshrrev_b32_e32 v5, 2, v5
	v_add_u32_e32 v5, v5, v38
	v_add_co_u32_e32 v2, vcc, v2, v39
	s_nop 1
	v_addc_co_u32_e32 v3, vcc, 0, v3, vcc
	v_add_co_u32_e32 v0, vcc, v0, v5
	s_nop 1
	v_addc_co_u32_e32 v1, vcc, 0, v1, vcc
	v_mov_b32_e32 v252, 0x43dc0000
	s_and_b64 vcc, exec, s[34:35]
	s_waitcnt vmcnt(16)
	v_lshlrev_b32_e32 v168, 16, v204
	v_and_b32_e32 v169, 0xffff0000, v204
	v_lshlrev_b32_e32 v170, 16, v205
	v_and_b32_e32 v171, 0xffff0000, v205
	v_lshlrev_b32_e32 v172, 16, v206
	v_and_b32_e32 v173, 0xffff0000, v206
	v_lshlrev_b32_e32 v174, 16, v207
	v_and_b32_e32 v175, 0xffff0000, v207
	v_pk_mul_f32 v[168:169], v[4:5], v[168:169] op_sel_hi:[0,1]
	v_pk_mul_f32 v[170:171], v[4:5], v[170:171] op_sel_hi:[0,1]
	v_pk_fma_f32 v[164:165], v[184:185], v[164:165], v[168:169] op_sel_hi:[0,1,1]
	v_pk_fma_f32 v[166:167], v[184:185], v[166:167], v[170:171] op_sel_hi:[0,1,1]
	v_pk_mul_f32 v[164:165], v[164:165], v[172:173]
	v_pk_mul_f32 v[166:167], v[166:167], v[174:175]
	v_cvt_pk_bf16_f32 v240, v164, v165
	v_cvt_pk_bf16_f32 v241, v166, v167
	v_lshlrev_b32_e32 v168, 16, v208
	v_and_b32_e32 v169, 0xffff0000, v208
	v_lshlrev_b32_e32 v170, 16, v209
	v_and_b32_e32 v171, 0xffff0000, v209
	v_lshlrev_b32_e32 v172, 16, v210
	v_and_b32_e32 v173, 0xffff0000, v210
	v_lshlrev_b32_e32 v174, 16, v211
	v_and_b32_e32 v175, 0xffff0000, v211
	v_pk_mul_f32 v[168:169], v[4:5], v[168:169] op_sel_hi:[0,1]
	v_pk_mul_f32 v[170:171], v[4:5], v[170:171] op_sel_hi:[0,1]
	v_pk_fma_f32 v[160:161], v[184:185], v[160:161], v[168:169] op_sel_hi:[0,1,1]
	v_pk_fma_f32 v[162:163], v[184:185], v[162:163], v[170:171] op_sel_hi:[0,1,1]
	v_pk_mul_f32 v[160:161], v[160:161], v[172:173]
	v_pk_mul_f32 v[162:163], v[162:163], v[174:175]
	v_cvt_pk_bf16_f32 v242, v160, v161
	v_cvt_pk_bf16_f32 v243, v162, v163
	s_nop 1
	v_permlane16_swap_b32_e32 v240, v242
	v_permlane16_swap_b32_e32 v241, v243
	global_store_dwordx4 v[2:3], v[240:243], off
	s_cbranch_vccz .Lt8e_0_0
	v_med3_f32 v248, v164, s77, v252
	v_med3_f32 v249, v165, s77, v252
	v_med3_f32 v250, v166, s77, v252
	v_med3_f32 v251, v167, s77, v252
	v_mov_b32_e32 v246, v245
	v_cvt_pk_fp8_f32 v246, v248, v249
	v_cvt_pk_fp8_f32 v246, v250, v251 op_sel:[0,0,1]
	v_med3_f32 v248, v160, s77, v252
	v_med3_f32 v249, v161, s77, v252
	v_med3_f32 v250, v162, s77, v252
	v_med3_f32 v251, v163, s77, v252
	v_mov_b32_e32 v247, v245
	v_cvt_pk_fp8_f32 v247, v248, v249
	v_cvt_pk_fp8_f32 v247, v250, v251 op_sel:[0,0,1]
	s_nop 1
	v_permlane16_swap_b32_e32 v246, v247
	global_store_dwordx2 v[0:1], v[246:247], off
.Lt8e_0_0:
	v_lshlrev_b32_e32 v168, 16, v212
	v_and_b32_e32 v169, 0xffff0000, v212
	v_lshlrev_b32_e32 v170, 16, v213
	v_and_b32_e32 v171, 0xffff0000, v213
	v_lshlrev_b32_e32 v172, 16, v214
	v_and_b32_e32 v173, 0xffff0000, v214
	v_lshlrev_b32_e32 v174, 16, v215
	v_and_b32_e32 v175, 0xffff0000, v215
	v_pk_mul_f32 v[168:169], v[4:5], v[168:169] op_sel_hi:[0,1]
	v_pk_mul_f32 v[170:171], v[4:5], v[170:171] op_sel_hi:[0,1]
	v_pk_fma_f32 v[156:157], v[184:185], v[156:157], v[168:169] op_sel_hi:[0,1,1]
	v_pk_fma_f32 v[158:159], v[184:185], v[158:159], v[170:171] op_sel_hi:[0,1,1]
	v_pk_mul_f32 v[156:157], v[156:157], v[172:173]
	v_pk_mul_f32 v[158:159], v[158:159], v[174:175]
	v_cvt_pk_bf16_f32 v240, v156, v157
	v_cvt_pk_bf16_f32 v241, v158, v159
	v_lshlrev_b32_e32 v168, 16, v216
	v_and_b32_e32 v169, 0xffff0000, v216
	v_lshlrev_b32_e32 v170, 16, v217
	v_and_b32_e32 v171, 0xffff0000, v217
	v_lshlrev_b32_e32 v172, 16, v218
	v_and_b32_e32 v173, 0xffff0000, v218
	v_lshlrev_b32_e32 v174, 16, v219
	v_and_b32_e32 v175, 0xffff0000, v219
	v_pk_mul_f32 v[168:169], v[4:5], v[168:169] op_sel_hi:[0,1]
	v_pk_mul_f32 v[170:171], v[4:5], v[170:171] op_sel_hi:[0,1]
	v_pk_fma_f32 v[152:153], v[184:185], v[152:153], v[168:169] op_sel_hi:[0,1,1]
	v_pk_fma_f32 v[154:155], v[184:185], v[154:155], v[170:171] op_sel_hi:[0,1,1]
	v_pk_mul_f32 v[152:153], v[152:153], v[172:173]
	v_pk_mul_f32 v[154:155], v[154:155], v[174:175]
	v_cvt_pk_bf16_f32 v242, v152, v153
	v_cvt_pk_bf16_f32 v243, v154, v155
	s_nop 1
	v_permlane16_swap_b32_e32 v240, v242
	v_permlane16_swap_b32_e32 v241, v243
	global_store_dwordx4 v[2:3], v[240:243], off offset:64
	s_cbranch_vccz .Lt8e_0_1
	v_med3_f32 v248, v156, s77, v252
	v_med3_f32 v249, v157, s77, v252
	v_med3_f32 v250, v158, s77, v252
	v_med3_f32 v251, v159, s77, v252
	v_mov_b32_e32 v246, v245
	v_cvt_pk_fp8_f32 v246, v248, v249
	v_cvt_pk_fp8_f32 v246, v250, v251 op_sel:[0,0,1]
	v_med3_f32 v248, v152, s77, v252
	v_med3_f32 v249, v153, s77, v252
	v_med3_f32 v250, v154, s77, v252
	v_med3_f32 v251, v155, s77, v252
	v_mov_b32_e32 v247, v245
	v_cvt_pk_fp8_f32 v247, v248, v249
	v_cvt_pk_fp8_f32 v247, v250, v251 op_sel:[0,0,1]
	s_nop 1
	v_permlane16_swap_b32_e32 v246, v247
	global_store_dwordx2 v[0:1], v[246:247], off offset:32
.Lt8e_0_1:
	v_lshlrev_b32_e32 v168, 16, v220
	v_and_b32_e32 v169, 0xffff0000, v220
	v_lshlrev_b32_e32 v170, 16, v221
	v_and_b32_e32 v171, 0xffff0000, v221
	v_lshlrev_b32_e32 v172, 16, v222
	v_and_b32_e32 v173, 0xffff0000, v222
	v_lshlrev_b32_e32 v174, 16, v223
	v_and_b32_e32 v175, 0xffff0000, v223
	v_pk_mul_f32 v[168:169], v[4:5], v[168:169] op_sel_hi:[0,1]
	v_pk_mul_f32 v[170:171], v[4:5], v[170:171] op_sel_hi:[0,1]
	v_pk_fma_f32 v[148:149], v[184:185], v[148:149], v[168:169] op_sel_hi:[0,1,1]
	v_pk_fma_f32 v[150:151], v[184:185], v[150:151], v[170:171] op_sel_hi:[0,1,1]
	v_pk_mul_f32 v[148:149], v[148:149], v[172:173]
	v_pk_mul_f32 v[150:151], v[150:151], v[174:175]
	v_cvt_pk_bf16_f32 v240, v148, v149
	v_cvt_pk_bf16_f32 v241, v150, v151
	v_lshlrev_b32_e32 v168, 16, v224
	v_and_b32_e32 v169, 0xffff0000, v224
	v_lshlrev_b32_e32 v170, 16, v225
	v_and_b32_e32 v171, 0xffff0000, v225
	v_lshlrev_b32_e32 v172, 16, v226
	v_and_b32_e32 v173, 0xffff0000, v226
	v_lshlrev_b32_e32 v174, 16, v227
	v_and_b32_e32 v175, 0xffff0000, v227
	v_pk_mul_f32 v[168:169], v[4:5], v[168:169] op_sel_hi:[0,1]
	v_pk_mul_f32 v[170:171], v[4:5], v[170:171] op_sel_hi:[0,1]
	v_pk_fma_f32 v[144:145], v[184:185], v[144:145], v[168:169] op_sel_hi:[0,1,1]
	v_pk_fma_f32 v[146:147], v[184:185], v[146:147], v[170:171] op_sel_hi:[0,1,1]
	v_pk_mul_f32 v[144:145], v[144:145], v[172:173]
	v_pk_mul_f32 v[146:147], v[146:147], v[174:175]
	v_cvt_pk_bf16_f32 v242, v144, v145
	v_cvt_pk_bf16_f32 v243, v146, v147
	s_nop 1
	v_permlane16_swap_b32_e32 v240, v242
	v_permlane16_swap_b32_e32 v241, v243
	global_store_dwordx4 v[2:3], v[240:243], off offset:128
	s_cbranch_vccz .Lt8e_0_2
	v_med3_f32 v248, v148, s77, v252
	v_med3_f32 v249, v149, s77, v252
	v_med3_f32 v250, v150, s77, v252
	v_med3_f32 v251, v151, s77, v252
	v_mov_b32_e32 v246, v245
	v_cvt_pk_fp8_f32 v246, v248, v249
	v_cvt_pk_fp8_f32 v246, v250, v251 op_sel:[0,0,1]
	v_med3_f32 v248, v144, s77, v252
	v_med3_f32 v249, v145, s77, v252
	v_med3_f32 v250, v146, s77, v252
	v_med3_f32 v251, v147, s77, v252
	v_mov_b32_e32 v247, v245
	v_cvt_pk_fp8_f32 v247, v248, v249
	v_cvt_pk_fp8_f32 v247, v250, v251 op_sel:[0,0,1]
	s_nop 1
	v_permlane16_swap_b32_e32 v246, v247
	global_store_dwordx2 v[0:1], v[246:247], off offset:64
.Lt8e_0_2:
	v_lshlrev_b32_e32 v168, 16, v228
	v_and_b32_e32 v169, 0xffff0000, v228
	v_lshlrev_b32_e32 v170, 16, v229
	v_and_b32_e32 v171, 0xffff0000, v229
	v_lshlrev_b32_e32 v172, 16, v230
	v_and_b32_e32 v173, 0xffff0000, v230
	v_lshlrev_b32_e32 v174, 16, v231
	v_and_b32_e32 v175, 0xffff0000, v231
	v_pk_mul_f32 v[168:169], v[4:5], v[168:169] op_sel_hi:[0,1]
	v_pk_mul_f32 v[170:171], v[4:5], v[170:171] op_sel_hi:[0,1]
	v_pk_fma_f32 v[140:141], v[184:185], v[140:141], v[168:169] op_sel_hi:[0,1,1]
	v_pk_fma_f32 v[142:143], v[184:185], v[142:143], v[170:171] op_sel_hi:[0,1,1]
	v_pk_mul_f32 v[140:141], v[140:141], v[172:173]
	v_pk_mul_f32 v[142:143], v[142:143], v[174:175]
	v_cvt_pk_bf16_f32 v240, v140, v141
	v_cvt_pk_bf16_f32 v241, v142, v143
	v_lshlrev_b32_e32 v168, 16, v232
	v_and_b32_e32 v169, 0xffff0000, v232
	v_lshlrev_b32_e32 v170, 16, v233
	v_and_b32_e32 v171, 0xffff0000, v233
	v_lshlrev_b32_e32 v172, 16, v234
	v_and_b32_e32 v173, 0xffff0000, v234
	v_lshlrev_b32_e32 v174, 16, v235
	v_and_b32_e32 v175, 0xffff0000, v235
	v_pk_mul_f32 v[168:169], v[4:5], v[168:169] op_sel_hi:[0,1]
	v_pk_mul_f32 v[170:171], v[4:5], v[170:171] op_sel_hi:[0,1]
	v_pk_fma_f32 v[136:137], v[184:185], v[136:137], v[168:169] op_sel_hi:[0,1,1]
	v_pk_fma_f32 v[138:139], v[184:185], v[138:139], v[170:171] op_sel_hi:[0,1,1]
	v_pk_mul_f32 v[136:137], v[136:137], v[172:173]
	v_pk_mul_f32 v[138:139], v[138:139], v[174:175]
	v_cvt_pk_bf16_f32 v242, v136, v137
	v_cvt_pk_bf16_f32 v243, v138, v139
	s_nop 1
	v_permlane16_swap_b32_e32 v240, v242
	v_permlane16_swap_b32_e32 v241, v243
	global_store_dwordx4 v[2:3], v[240:243], off offset:192
	s_cbranch_vccz .Lt8e_0_3
	v_med3_f32 v248, v140, s77, v252
	v_med3_f32 v249, v141, s77, v252
	v_med3_f32 v250, v142, s77, v252
	v_med3_f32 v251, v143, s77, v252
	v_mov_b32_e32 v246, v245
	v_cvt_pk_fp8_f32 v246, v248, v249
	v_cvt_pk_fp8_f32 v246, v250, v251 op_sel:[0,0,1]
	v_med3_f32 v248, v136, s77, v252
	v_med3_f32 v249, v137, s77, v252
	v_med3_f32 v250, v138, s77, v252
	v_med3_f32 v251, v139, s77, v252
	v_mov_b32_e32 v247, v245
	v_cvt_pk_fp8_f32 v247, v248, v249
	v_cvt_pk_fp8_f32 v247, v250, v251 op_sel:[0,0,1]
	s_nop 1
	v_permlane16_swap_b32_e32 v246, v247
	global_store_dwordx2 v[0:1], v[246:247], off offset:96
.Lt8e_0_3:
	global_load_dwordx2 v[204:205], v[8:9], off offset:512
	global_load_dwordx2 v[206:207], v[6:7], off offset:512
	global_load_dwordx2 v[208:209], v[8:9], off offset:544
	global_load_dwordx2 v[210:211], v[6:7], off offset:544
	global_load_dwordx2 v[212:213], v[8:9], off offset:576
	global_load_dwordx2 v[214:215], v[6:7], off offset:576
	global_load_dwordx2 v[216:217], v[8:9], off offset:608
	global_load_dwordx2 v[218:219], v[6:7], off offset:608
	global_load_dwordx2 v[220:221], v[8:9], off offset:640
	global_load_dwordx2 v[222:223], v[6:7], off offset:640
	global_load_dwordx2 v[224:225], v[8:9], off offset:672
	global_load_dwordx2 v[226:227], v[6:7], off offset:672
	global_load_dwordx2 v[228:229], v[8:9], off offset:704
	global_load_dwordx2 v[230:231], v[6:7], off offset:704
	global_load_dwordx2 v[232:233], v[8:9], off offset:736
	global_load_dwordx2 v[234:235], v[6:7], off offset:736
	s_waitcnt vmcnt(20)
	v_lshlrev_b32_e32 v168, 16, v10
	v_and_b32_e32 v169, 0xffff0000, v10
	v_lshlrev_b32_e32 v170, 16, v11
	v_and_b32_e32 v171, 0xffff0000, v11
	v_lshlrev_b32_e32 v172, 16, v12
	v_and_b32_e32 v173, 0xffff0000, v12
	v_lshlrev_b32_e32 v174, 16, v13
	v_and_b32_e32 v175, 0xffff0000, v13
	v_pk_mul_f32 v[168:169], v[4:5], v[168:169] op_sel_hi:[0,1]
	v_pk_mul_f32 v[170:171], v[4:5], v[170:171] op_sel_hi:[0,1]
	v_pk_fma_f32 v[132:133], v[184:185], v[132:133], v[168:169] op_sel_hi:[0,1,1]
	v_pk_fma_f32 v[134:135], v[184:185], v[134:135], v[170:171] op_sel_hi:[0,1,1]
	v_pk_mul_f32 v[132:133], v[132:133], v[172:173]
	v_pk_mul_f32 v[134:135], v[134:135], v[174:175]
	v_cvt_pk_bf16_f32 v240, v132, v133
	v_cvt_pk_bf16_f32 v241, v134, v135
	v_lshlrev_b32_e32 v168, 16, v14
	v_and_b32_e32 v169, 0xffff0000, v14
	v_lshlrev_b32_e32 v170, 16, v15
	v_and_b32_e32 v171, 0xffff0000, v15
	v_lshlrev_b32_e32 v172, 16, v16
	v_and_b32_e32 v173, 0xffff0000, v16
	v_lshlrev_b32_e32 v174, 16, v17
	v_and_b32_e32 v175, 0xffff0000, v17
	v_pk_mul_f32 v[168:169], v[4:5], v[168:169] op_sel_hi:[0,1]
	v_pk_mul_f32 v[170:171], v[4:5], v[170:171] op_sel_hi:[0,1]
	v_pk_fma_f32 v[128:129], v[184:185], v[128:129], v[168:169] op_sel_hi:[0,1,1]
	v_pk_fma_f32 v[130:131], v[184:185], v[130:131], v[170:171] op_sel_hi:[0,1,1]
	v_pk_mul_f32 v[128:129], v[128:129], v[172:173]
	v_pk_mul_f32 v[130:131], v[130:131], v[174:175]
	v_cvt_pk_bf16_f32 v242, v128, v129
	v_cvt_pk_bf16_f32 v243, v130, v131
	s_nop 1
	v_permlane16_swap_b32_e32 v240, v242
	v_permlane16_swap_b32_e32 v241, v243
	global_store_dwordx4 v[2:3], v[240:243], off offset:256
	s_cbranch_vccz .Lt8e_1_0
	v_med3_f32 v248, v132, s77, v252
	v_med3_f32 v249, v133, s77, v252
	v_med3_f32 v250, v134, s77, v252
	v_med3_f32 v251, v135, s77, v252
	v_mov_b32_e32 v246, v245
	v_cvt_pk_fp8_f32 v246, v248, v249
	v_cvt_pk_fp8_f32 v246, v250, v251 op_sel:[0,0,1]
	v_med3_f32 v248, v128, s77, v252
	v_med3_f32 v249, v129, s77, v252
	v_med3_f32 v250, v130, s77, v252
	v_med3_f32 v251, v131, s77, v252
	v_mov_b32_e32 v247, v245
	v_cvt_pk_fp8_f32 v247, v248, v249
	v_cvt_pk_fp8_f32 v247, v250, v251 op_sel:[0,0,1]
	s_nop 1
	v_permlane16_swap_b32_e32 v246, v247
	global_store_dwordx2 v[0:1], v[246:247], off offset:128
.Lt8e_1_0:
	v_lshlrev_b32_e32 v168, 16, v18
	v_and_b32_e32 v169, 0xffff0000, v18
	v_lshlrev_b32_e32 v170, 16, v19
	v_and_b32_e32 v171, 0xffff0000, v19
	v_lshlrev_b32_e32 v172, 16, v20
	v_and_b32_e32 v173, 0xffff0000, v20
	v_lshlrev_b32_e32 v174, 16, v21
	v_and_b32_e32 v175, 0xffff0000, v21
	v_pk_mul_f32 v[168:169], v[4:5], v[168:169] op_sel_hi:[0,1]
	v_pk_mul_f32 v[170:171], v[4:5], v[170:171] op_sel_hi:[0,1]
	v_pk_fma_f32 v[124:125], v[184:185], v[124:125], v[168:169] op_sel_hi:[0,1,1]
	v_pk_fma_f32 v[126:127], v[184:185], v[126:127], v[170:171] op_sel_hi:[0,1,1]
	v_pk_mul_f32 v[124:125], v[124:125], v[172:173]
	v_pk_mul_f32 v[126:127], v[126:127], v[174:175]
	v_cvt_pk_bf16_f32 v240, v124, v125
	v_cvt_pk_bf16_f32 v241, v126, v127
	v_lshlrev_b32_e32 v168, 16, v22
	v_and_b32_e32 v169, 0xffff0000, v22
	v_lshlrev_b32_e32 v170, 16, v23
	v_and_b32_e32 v171, 0xffff0000, v23
	v_lshlrev_b32_e32 v172, 16, v24
	v_and_b32_e32 v173, 0xffff0000, v24
	v_lshlrev_b32_e32 v174, 16, v25
	v_and_b32_e32 v175, 0xffff0000, v25
	v_pk_mul_f32 v[168:169], v[4:5], v[168:169] op_sel_hi:[0,1]
	v_pk_mul_f32 v[170:171], v[4:5], v[170:171] op_sel_hi:[0,1]
	v_pk_fma_f32 v[120:121], v[184:185], v[120:121], v[168:169] op_sel_hi:[0,1,1]
	v_pk_fma_f32 v[122:123], v[184:185], v[122:123], v[170:171] op_sel_hi:[0,1,1]
	v_pk_mul_f32 v[120:121], v[120:121], v[172:173]
	v_pk_mul_f32 v[122:123], v[122:123], v[174:175]
	v_cvt_pk_bf16_f32 v242, v120, v121
	v_cvt_pk_bf16_f32 v243, v122, v123
	s_nop 1
	v_permlane16_swap_b32_e32 v240, v242
	v_permlane16_swap_b32_e32 v241, v243
	global_store_dwordx4 v[2:3], v[240:243], off offset:320
	s_cbranch_vccz .Lt8e_1_1
	v_med3_f32 v248, v124, s77, v252
	v_med3_f32 v249, v125, s77, v252
	v_med3_f32 v250, v126, s77, v252
	v_med3_f32 v251, v127, s77, v252
	v_mov_b32_e32 v246, v245
	v_cvt_pk_fp8_f32 v246, v248, v249
	v_cvt_pk_fp8_f32 v246, v250, v251 op_sel:[0,0,1]
	v_med3_f32 v248, v120, s77, v252
	v_med3_f32 v249, v121, s77, v252
	v_med3_f32 v250, v122, s77, v252
	v_med3_f32 v251, v123, s77, v252
	v_mov_b32_e32 v247, v245
	v_cvt_pk_fp8_f32 v247, v248, v249
	v_cvt_pk_fp8_f32 v247, v250, v251 op_sel:[0,0,1]
	s_nop 1
	v_permlane16_swap_b32_e32 v246, v247
	global_store_dwordx2 v[0:1], v[246:247], off offset:160
.Lt8e_1_1:
	v_lshlrev_b32_e32 v168, 16, v26
	v_and_b32_e32 v169, 0xffff0000, v26
	v_lshlrev_b32_e32 v170, 16, v27
	v_and_b32_e32 v171, 0xffff0000, v27
	v_lshlrev_b32_e32 v172, 16, v28
	v_and_b32_e32 v173, 0xffff0000, v28
	v_lshlrev_b32_e32 v174, 16, v29
	v_and_b32_e32 v175, 0xffff0000, v29
	v_pk_mul_f32 v[168:169], v[4:5], v[168:169] op_sel_hi:[0,1]
	v_pk_mul_f32 v[170:171], v[4:5], v[170:171] op_sel_hi:[0,1]
	v_pk_fma_f32 v[116:117], v[184:185], v[116:117], v[168:169] op_sel_hi:[0,1,1]
	v_pk_fma_f32 v[118:119], v[184:185], v[118:119], v[170:171] op_sel_hi:[0,1,1]
	v_pk_mul_f32 v[116:117], v[116:117], v[172:173]
	v_pk_mul_f32 v[118:119], v[118:119], v[174:175]
	v_cvt_pk_bf16_f32 v240, v116, v117
	v_cvt_pk_bf16_f32 v241, v118, v119
	v_lshlrev_b32_e32 v168, 16, v30
	v_and_b32_e32 v169, 0xffff0000, v30
	v_lshlrev_b32_e32 v170, 16, v31
	v_and_b32_e32 v171, 0xffff0000, v31
	v_lshlrev_b32_e32 v172, 16, v32
	v_and_b32_e32 v173, 0xffff0000, v32
	v_lshlrev_b32_e32 v174, 16, v33
	v_and_b32_e32 v175, 0xffff0000, v33
	v_pk_mul_f32 v[168:169], v[4:5], v[168:169] op_sel_hi:[0,1]
	v_pk_mul_f32 v[170:171], v[4:5], v[170:171] op_sel_hi:[0,1]
	v_pk_fma_f32 v[112:113], v[184:185], v[112:113], v[168:169] op_sel_hi:[0,1,1]
	v_pk_fma_f32 v[114:115], v[184:185], v[114:115], v[170:171] op_sel_hi:[0,1,1]
	v_pk_mul_f32 v[112:113], v[112:113], v[172:173]
	v_pk_mul_f32 v[114:115], v[114:115], v[174:175]
	v_cvt_pk_bf16_f32 v242, v112, v113
	v_cvt_pk_bf16_f32 v243, v114, v115
	s_nop 1
	v_permlane16_swap_b32_e32 v240, v242
	v_permlane16_swap_b32_e32 v241, v243
	global_store_dwordx4 v[2:3], v[240:243], off offset:384
	s_cbranch_vccz .Lt8e_1_2
	v_med3_f32 v248, v116, s77, v252
	v_med3_f32 v249, v117, s77, v252
	v_med3_f32 v250, v118, s77, v252
	v_med3_f32 v251, v119, s77, v252
	v_mov_b32_e32 v246, v245
	v_cvt_pk_fp8_f32 v246, v248, v249
	v_cvt_pk_fp8_f32 v246, v250, v251 op_sel:[0,0,1]
	v_med3_f32 v248, v112, s77, v252
	v_med3_f32 v249, v113, s77, v252
	v_med3_f32 v250, v114, s77, v252
	v_med3_f32 v251, v115, s77, v252
	v_mov_b32_e32 v247, v245
	v_cvt_pk_fp8_f32 v247, v248, v249
	v_cvt_pk_fp8_f32 v247, v250, v251 op_sel:[0,0,1]
	s_nop 1
	v_permlane16_swap_b32_e32 v246, v247
	global_store_dwordx2 v[0:1], v[246:247], off offset:192
.Lt8e_1_2:
	v_lshlrev_b32_e32 v168, 16, v34
	v_and_b32_e32 v169, 0xffff0000, v34
	v_lshlrev_b32_e32 v170, 16, v35
	v_and_b32_e32 v171, 0xffff0000, v35
	v_lshlrev_b32_e32 v172, 16, v36
	v_and_b32_e32 v173, 0xffff0000, v36
	v_lshlrev_b32_e32 v174, 16, v37
	v_and_b32_e32 v175, 0xffff0000, v37
	v_pk_mul_f32 v[168:169], v[4:5], v[168:169] op_sel_hi:[0,1]
	v_pk_mul_f32 v[170:171], v[4:5], v[170:171] op_sel_hi:[0,1]
	v_pk_fma_f32 v[108:109], v[184:185], v[108:109], v[168:169] op_sel_hi:[0,1,1]
	v_pk_fma_f32 v[110:111], v[184:185], v[110:111], v[170:171] op_sel_hi:[0,1,1]
	v_pk_mul_f32 v[108:109], v[108:109], v[172:173]
	v_pk_mul_f32 v[110:111], v[110:111], v[174:175]
	v_cvt_pk_bf16_f32 v240, v108, v109
	v_cvt_pk_bf16_f32 v241, v110, v111
	v_lshlrev_b32_e32 v168, 16, v236
	v_and_b32_e32 v169, 0xffff0000, v236
	v_lshlrev_b32_e32 v170, 16, v237
	v_and_b32_e32 v171, 0xffff0000, v237
	v_lshlrev_b32_e32 v172, 16, v238
	v_and_b32_e32 v173, 0xffff0000, v238
	v_lshlrev_b32_e32 v174, 16, v239
	v_and_b32_e32 v175, 0xffff0000, v239
	v_pk_mul_f32 v[168:169], v[4:5], v[168:169] op_sel_hi:[0,1]
	v_pk_mul_f32 v[170:171], v[4:5], v[170:171] op_sel_hi:[0,1]
	v_pk_fma_f32 v[104:105], v[184:185], v[104:105], v[168:169] op_sel_hi:[0,1,1]
	v_pk_fma_f32 v[106:107], v[184:185], v[106:107], v[170:171] op_sel_hi:[0,1,1]
	v_pk_mul_f32 v[104:105], v[104:105], v[172:173]
	v_pk_mul_f32 v[106:107], v[106:107], v[174:175]
	v_cvt_pk_bf16_f32 v242, v104, v105
	v_cvt_pk_bf16_f32 v243, v106, v107
	s_nop 1
	v_permlane16_swap_b32_e32 v240, v242
	v_permlane16_swap_b32_e32 v241, v243
	global_store_dwordx4 v[2:3], v[240:243], off offset:448
	s_cbranch_vccz .Lt8e_1_3
	v_med3_f32 v248, v108, s77, v252
	v_med3_f32 v249, v109, s77, v252
	v_med3_f32 v250, v110, s77, v252
	v_med3_f32 v251, v111, s77, v252
	v_mov_b32_e32 v246, v245
	v_cvt_pk_fp8_f32 v246, v248, v249
	v_cvt_pk_fp8_f32 v246, v250, v251 op_sel:[0,0,1]
	v_med3_f32 v248, v104, s77, v252
	v_med3_f32 v249, v105, s77, v252
	v_med3_f32 v250, v106, s77, v252
	v_med3_f32 v251, v107, s77, v252
	v_mov_b32_e32 v247, v245
	v_cvt_pk_fp8_f32 v247, v248, v249
	v_cvt_pk_fp8_f32 v247, v250, v251 op_sel:[0,0,1]
	s_nop 1
	v_permlane16_swap_b32_e32 v246, v247
	global_store_dwordx2 v[0:1], v[246:247], off offset:224
.Lt8e_1_3:
	global_load_dwordx2 v[10:11], v[8:9], off offset:768
	global_load_dwordx2 v[12:13], v[6:7], off offset:768
	global_load_dwordx2 v[14:15], v[8:9], off offset:800
	global_load_dwordx2 v[16:17], v[6:7], off offset:800
	global_load_dwordx2 v[18:19], v[8:9], off offset:832
	global_load_dwordx2 v[20:21], v[6:7], off offset:832
	global_load_dwordx2 v[22:23], v[8:9], off offset:864
	global_load_dwordx2 v[24:25], v[6:7], off offset:864
	global_load_dwordx2 v[26:27], v[8:9], off offset:896
	global_load_dwordx2 v[28:29], v[6:7], off offset:896
	global_load_dwordx2 v[30:31], v[8:9], off offset:928
	global_load_dwordx2 v[32:33], v[6:7], off offset:928
	global_load_dwordx2 v[34:35], v[8:9], off offset:960
	global_load_dwordx2 v[36:37], v[6:7], off offset:960
	global_load_dwordx2 v[236:237], v[8:9], off offset:992
	global_load_dwordx2 v[238:239], v[6:7], off offset:992
	s_waitcnt vmcnt(20)
	v_lshlrev_b32_e32 v168, 16, v204
	v_and_b32_e32 v169, 0xffff0000, v204
	v_lshlrev_b32_e32 v170, 16, v205
	v_and_b32_e32 v171, 0xffff0000, v205
	v_lshlrev_b32_e32 v172, 16, v206
	v_and_b32_e32 v173, 0xffff0000, v206
	v_lshlrev_b32_e32 v174, 16, v207
	v_and_b32_e32 v175, 0xffff0000, v207
	v_pk_mul_f32 v[168:169], v[4:5], v[168:169] op_sel_hi:[0,1]
	v_pk_mul_f32 v[170:171], v[4:5], v[170:171] op_sel_hi:[0,1]
	v_pk_fma_f32 v[100:101], v[184:185], v[100:101], v[168:169] op_sel_hi:[0,1,1]
	v_pk_fma_f32 v[102:103], v[184:185], v[102:103], v[170:171] op_sel_hi:[0,1,1]
	v_pk_mul_f32 v[100:101], v[100:101], v[172:173]
	v_pk_mul_f32 v[102:103], v[102:103], v[174:175]
	v_cvt_pk_bf16_f32 v240, v100, v101
	v_cvt_pk_bf16_f32 v241, v102, v103
	v_lshlrev_b32_e32 v168, 16, v208
	v_and_b32_e32 v169, 0xffff0000, v208
	v_lshlrev_b32_e32 v170, 16, v209
	v_and_b32_e32 v171, 0xffff0000, v209
	v_lshlrev_b32_e32 v172, 16, v210
	v_and_b32_e32 v173, 0xffff0000, v210
	v_lshlrev_b32_e32 v174, 16, v211
	v_and_b32_e32 v175, 0xffff0000, v211
	v_pk_mul_f32 v[168:169], v[4:5], v[168:169] op_sel_hi:[0,1]
	v_pk_mul_f32 v[170:171], v[4:5], v[170:171] op_sel_hi:[0,1]
	v_pk_fma_f32 v[96:97], v[184:185], v[96:97], v[168:169] op_sel_hi:[0,1,1]
	v_pk_fma_f32 v[98:99], v[184:185], v[98:99], v[170:171] op_sel_hi:[0,1,1]
	v_pk_mul_f32 v[96:97], v[96:97], v[172:173]
	v_pk_mul_f32 v[98:99], v[98:99], v[174:175]
	v_cvt_pk_bf16_f32 v242, v96, v97
	v_cvt_pk_bf16_f32 v243, v98, v99
	s_nop 1
	v_permlane16_swap_b32_e32 v240, v242
	v_permlane16_swap_b32_e32 v241, v243
	global_store_dwordx4 v[2:3], v[240:243], off offset:512
	s_cbranch_vccz .Lt8e_2_0
	v_med3_f32 v248, v100, s77, v252
	v_med3_f32 v249, v101, s77, v252
	v_med3_f32 v250, v102, s77, v252
	v_med3_f32 v251, v103, s77, v252
	v_mov_b32_e32 v246, v245
	v_cvt_pk_fp8_f32 v246, v248, v249
	v_cvt_pk_fp8_f32 v246, v250, v251 op_sel:[0,0,1]
	v_med3_f32 v248, v96, s77, v252
	v_med3_f32 v249, v97, s77, v252
	v_med3_f32 v250, v98, s77, v252
	v_med3_f32 v251, v99, s77, v252
	v_mov_b32_e32 v247, v245
	v_cvt_pk_fp8_f32 v247, v248, v249
	v_cvt_pk_fp8_f32 v247, v250, v251 op_sel:[0,0,1]
	s_nop 1
	v_permlane16_swap_b32_e32 v246, v247
	global_store_dwordx2 v[0:1], v[246:247], off offset:256
.Lt8e_2_0:
	v_lshlrev_b32_e32 v168, 16, v212
	v_and_b32_e32 v169, 0xffff0000, v212
	v_lshlrev_b32_e32 v170, 16, v213
	v_and_b32_e32 v171, 0xffff0000, v213
	v_lshlrev_b32_e32 v172, 16, v214
	v_and_b32_e32 v173, 0xffff0000, v214
	v_lshlrev_b32_e32 v174, 16, v215
	v_and_b32_e32 v175, 0xffff0000, v215
	v_pk_mul_f32 v[168:169], v[4:5], v[168:169] op_sel_hi:[0,1]
	v_pk_mul_f32 v[170:171], v[4:5], v[170:171] op_sel_hi:[0,1]
	v_pk_fma_f32 v[92:93], v[184:185], v[92:93], v[168:169] op_sel_hi:[0,1,1]
	v_pk_fma_f32 v[94:95], v[184:185], v[94:95], v[170:171] op_sel_hi:[0,1,1]
	v_pk_mul_f32 v[92:93], v[92:93], v[172:173]
	v_pk_mul_f32 v[94:95], v[94:95], v[174:175]
	v_cvt_pk_bf16_f32 v240, v92, v93
	v_cvt_pk_bf16_f32 v241, v94, v95
	v_lshlrev_b32_e32 v168, 16, v216
	v_and_b32_e32 v169, 0xffff0000, v216
	v_lshlrev_b32_e32 v170, 16, v217
	v_and_b32_e32 v171, 0xffff0000, v217
	v_lshlrev_b32_e32 v172, 16, v218
	v_and_b32_e32 v173, 0xffff0000, v218
	v_lshlrev_b32_e32 v174, 16, v219
	v_and_b32_e32 v175, 0xffff0000, v219
	v_pk_mul_f32 v[168:169], v[4:5], v[168:169] op_sel_hi:[0,1]
	v_pk_mul_f32 v[170:171], v[4:5], v[170:171] op_sel_hi:[0,1]
	v_pk_fma_f32 v[88:89], v[184:185], v[88:89], v[168:169] op_sel_hi:[0,1,1]
	v_pk_fma_f32 v[90:91], v[184:185], v[90:91], v[170:171] op_sel_hi:[0,1,1]
	v_pk_mul_f32 v[88:89], v[88:89], v[172:173]
	v_pk_mul_f32 v[90:91], v[90:91], v[174:175]
	v_cvt_pk_bf16_f32 v242, v88, v89
	v_cvt_pk_bf16_f32 v243, v90, v91
	s_nop 1
	v_permlane16_swap_b32_e32 v240, v242
	v_permlane16_swap_b32_e32 v241, v243
	global_store_dwordx4 v[2:3], v[240:243], off offset:576
	s_cbranch_vccz .Lt8e_2_1
	v_med3_f32 v248, v92, s77, v252
	v_med3_f32 v249, v93, s77, v252
	v_med3_f32 v250, v94, s77, v252
	v_med3_f32 v251, v95, s77, v252
	v_mov_b32_e32 v246, v245
	v_cvt_pk_fp8_f32 v246, v248, v249
	v_cvt_pk_fp8_f32 v246, v250, v251 op_sel:[0,0,1]
	v_med3_f32 v248, v88, s77, v252
	v_med3_f32 v249, v89, s77, v252
	v_med3_f32 v250, v90, s77, v252
	v_med3_f32 v251, v91, s77, v252
	v_mov_b32_e32 v247, v245
	v_cvt_pk_fp8_f32 v247, v248, v249
	v_cvt_pk_fp8_f32 v247, v250, v251 op_sel:[0,0,1]
	s_nop 1
	v_permlane16_swap_b32_e32 v246, v247
	global_store_dwordx2 v[0:1], v[246:247], off offset:288
.Lt8e_2_1:
	v_lshlrev_b32_e32 v168, 16, v220
	v_and_b32_e32 v169, 0xffff0000, v220
	v_lshlrev_b32_e32 v170, 16, v221
	v_and_b32_e32 v171, 0xffff0000, v221
	v_lshlrev_b32_e32 v172, 16, v222
	v_and_b32_e32 v173, 0xffff0000, v222
	v_lshlrev_b32_e32 v174, 16, v223
	v_and_b32_e32 v175, 0xffff0000, v223
	v_pk_mul_f32 v[168:169], v[4:5], v[168:169] op_sel_hi:[0,1]
	v_pk_mul_f32 v[170:171], v[4:5], v[170:171] op_sel_hi:[0,1]
	v_pk_fma_f32 v[84:85], v[184:185], v[84:85], v[168:169] op_sel_hi:[0,1,1]
	v_pk_fma_f32 v[86:87], v[184:185], v[86:87], v[170:171] op_sel_hi:[0,1,1]
	v_pk_mul_f32 v[84:85], v[84:85], v[172:173]
	v_pk_mul_f32 v[86:87], v[86:87], v[174:175]
	v_cvt_pk_bf16_f32 v240, v84, v85
	v_cvt_pk_bf16_f32 v241, v86, v87
	v_lshlrev_b32_e32 v168, 16, v224
	v_and_b32_e32 v169, 0xffff0000, v224
	v_lshlrev_b32_e32 v170, 16, v225
	v_and_b32_e32 v171, 0xffff0000, v225
	v_lshlrev_b32_e32 v172, 16, v226
	v_and_b32_e32 v173, 0xffff0000, v226
	v_lshlrev_b32_e32 v174, 16, v227
	v_and_b32_e32 v175, 0xffff0000, v227
	v_pk_mul_f32 v[168:169], v[4:5], v[168:169] op_sel_hi:[0,1]
	v_pk_mul_f32 v[170:171], v[4:5], v[170:171] op_sel_hi:[0,1]
	v_pk_fma_f32 v[80:81], v[184:185], v[80:81], v[168:169] op_sel_hi:[0,1,1]
	v_pk_fma_f32 v[82:83], v[184:185], v[82:83], v[170:171] op_sel_hi:[0,1,1]
	v_pk_mul_f32 v[80:81], v[80:81], v[172:173]
	v_pk_mul_f32 v[82:83], v[82:83], v[174:175]
	v_cvt_pk_bf16_f32 v242, v80, v81
	v_cvt_pk_bf16_f32 v243, v82, v83
	s_nop 1
	v_permlane16_swap_b32_e32 v240, v242
	v_permlane16_swap_b32_e32 v241, v243
	global_store_dwordx4 v[2:3], v[240:243], off offset:640
	s_cbranch_vccz .Lt8e_2_2
	v_med3_f32 v248, v84, s77, v252
	v_med3_f32 v249, v85, s77, v252
	v_med3_f32 v250, v86, s77, v252
	v_med3_f32 v251, v87, s77, v252
	v_mov_b32_e32 v246, v245
	v_cvt_pk_fp8_f32 v246, v248, v249
	v_cvt_pk_fp8_f32 v246, v250, v251 op_sel:[0,0,1]
	v_med3_f32 v248, v80, s77, v252
	v_med3_f32 v249, v81, s77, v252
	v_med3_f32 v250, v82, s77, v252
	v_med3_f32 v251, v83, s77, v252
	v_mov_b32_e32 v247, v245
	v_cvt_pk_fp8_f32 v247, v248, v249
	v_cvt_pk_fp8_f32 v247, v250, v251 op_sel:[0,0,1]
	s_nop 1
	v_permlane16_swap_b32_e32 v246, v247
	global_store_dwordx2 v[0:1], v[246:247], off offset:320
.Lt8e_2_2:
	v_lshlrev_b32_e32 v168, 16, v228
	v_and_b32_e32 v169, 0xffff0000, v228
	v_lshlrev_b32_e32 v170, 16, v229
	v_and_b32_e32 v171, 0xffff0000, v229
	v_lshlrev_b32_e32 v172, 16, v230
	v_and_b32_e32 v173, 0xffff0000, v230
	v_lshlrev_b32_e32 v174, 16, v231
	v_and_b32_e32 v175, 0xffff0000, v231
	v_pk_mul_f32 v[168:169], v[4:5], v[168:169] op_sel_hi:[0,1]
	v_pk_mul_f32 v[170:171], v[4:5], v[170:171] op_sel_hi:[0,1]
	v_pk_fma_f32 v[76:77], v[184:185], v[76:77], v[168:169] op_sel_hi:[0,1,1]
	v_pk_fma_f32 v[78:79], v[184:185], v[78:79], v[170:171] op_sel_hi:[0,1,1]
	v_pk_mul_f32 v[76:77], v[76:77], v[172:173]
	v_pk_mul_f32 v[78:79], v[78:79], v[174:175]
	v_cvt_pk_bf16_f32 v240, v76, v77
	v_cvt_pk_bf16_f32 v241, v78, v79
	v_lshlrev_b32_e32 v168, 16, v232
	v_and_b32_e32 v169, 0xffff0000, v232
	v_lshlrev_b32_e32 v170, 16, v233
	v_and_b32_e32 v171, 0xffff0000, v233
	v_lshlrev_b32_e32 v172, 16, v234
	v_and_b32_e32 v173, 0xffff0000, v234
	v_lshlrev_b32_e32 v174, 16, v235
	v_and_b32_e32 v175, 0xffff0000, v235
	v_pk_mul_f32 v[168:169], v[4:5], v[168:169] op_sel_hi:[0,1]
	v_pk_mul_f32 v[170:171], v[4:5], v[170:171] op_sel_hi:[0,1]
	v_pk_fma_f32 v[72:73], v[184:185], v[72:73], v[168:169] op_sel_hi:[0,1,1]
	v_pk_fma_f32 v[74:75], v[184:185], v[74:75], v[170:171] op_sel_hi:[0,1,1]
	v_pk_mul_f32 v[72:73], v[72:73], v[172:173]
	v_pk_mul_f32 v[74:75], v[74:75], v[174:175]
	v_cvt_pk_bf16_f32 v242, v72, v73
	v_cvt_pk_bf16_f32 v243, v74, v75
	s_nop 1
	v_permlane16_swap_b32_e32 v240, v242
	v_permlane16_swap_b32_e32 v241, v243
	global_store_dwordx4 v[2:3], v[240:243], off offset:704
	s_cbranch_vccz .Lt8e_2_3
	v_med3_f32 v248, v76, s77, v252
	v_med3_f32 v249, v77, s77, v252
	v_med3_f32 v250, v78, s77, v252
	v_med3_f32 v251, v79, s77, v252
	v_mov_b32_e32 v246, v245
	v_cvt_pk_fp8_f32 v246, v248, v249
	v_cvt_pk_fp8_f32 v246, v250, v251 op_sel:[0,0,1]
	v_med3_f32 v248, v72, s77, v252
	v_med3_f32 v249, v73, s77, v252
	v_med3_f32 v250, v74, s77, v252
	v_med3_f32 v251, v75, s77, v252
	v_mov_b32_e32 v247, v245
	v_cvt_pk_fp8_f32 v247, v248, v249
	v_cvt_pk_fp8_f32 v247, v250, v251 op_sel:[0,0,1]
	s_nop 1
	v_permlane16_swap_b32_e32 v246, v247
	global_store_dwordx2 v[0:1], v[246:247], off offset:352
.Lt8e_2_3:
	s_waitcnt vmcnt(4)
	v_lshlrev_b32_e32 v168, 16, v10
	v_and_b32_e32 v169, 0xffff0000, v10
	v_lshlrev_b32_e32 v170, 16, v11
	v_and_b32_e32 v171, 0xffff0000, v11
	v_lshlrev_b32_e32 v172, 16, v12
	v_and_b32_e32 v173, 0xffff0000, v12
	v_lshlrev_b32_e32 v174, 16, v13
	v_and_b32_e32 v175, 0xffff0000, v13
	v_pk_mul_f32 v[168:169], v[4:5], v[168:169] op_sel_hi:[0,1]
	v_pk_mul_f32 v[170:171], v[4:5], v[170:171] op_sel_hi:[0,1]
	v_pk_fma_f32 v[68:69], v[184:185], v[68:69], v[168:169] op_sel_hi:[0,1,1]
	v_pk_fma_f32 v[70:71], v[184:185], v[70:71], v[170:171] op_sel_hi:[0,1,1]
	v_pk_mul_f32 v[68:69], v[68:69], v[172:173]
	v_pk_mul_f32 v[70:71], v[70:71], v[174:175]
	v_cvt_pk_bf16_f32 v240, v68, v69
	v_cvt_pk_bf16_f32 v241, v70, v71
	v_lshlrev_b32_e32 v168, 16, v14
	v_and_b32_e32 v169, 0xffff0000, v14
	v_lshlrev_b32_e32 v170, 16, v15
	v_and_b32_e32 v171, 0xffff0000, v15
	v_lshlrev_b32_e32 v172, 16, v16
	v_and_b32_e32 v173, 0xffff0000, v16
	v_lshlrev_b32_e32 v174, 16, v17
	v_and_b32_e32 v175, 0xffff0000, v17
	v_pk_mul_f32 v[168:169], v[4:5], v[168:169] op_sel_hi:[0,1]
	v_pk_mul_f32 v[170:171], v[4:5], v[170:171] op_sel_hi:[0,1]
	v_pk_fma_f32 v[64:65], v[184:185], v[64:65], v[168:169] op_sel_hi:[0,1,1]
	v_pk_fma_f32 v[66:67], v[184:185], v[66:67], v[170:171] op_sel_hi:[0,1,1]
	v_pk_mul_f32 v[64:65], v[64:65], v[172:173]
	v_pk_mul_f32 v[66:67], v[66:67], v[174:175]
	v_cvt_pk_bf16_f32 v242, v64, v65
	v_cvt_pk_bf16_f32 v243, v66, v67
	s_nop 1
	v_permlane16_swap_b32_e32 v240, v242
	v_permlane16_swap_b32_e32 v241, v243
	global_store_dwordx4 v[2:3], v[240:243], off offset:768
	s_cbranch_vccz .Lt8e_3_0
	v_med3_f32 v248, v68, s77, v252
	v_med3_f32 v249, v69, s77, v252
	v_med3_f32 v250, v70, s77, v252
	v_med3_f32 v251, v71, s77, v252
	v_mov_b32_e32 v246, v245
	v_cvt_pk_fp8_f32 v246, v248, v249
	v_cvt_pk_fp8_f32 v246, v250, v251 op_sel:[0,0,1]
	v_med3_f32 v248, v64, s77, v252
	v_med3_f32 v249, v65, s77, v252
	v_med3_f32 v250, v66, s77, v252
	v_med3_f32 v251, v67, s77, v252
	v_mov_b32_e32 v247, v245
	v_cvt_pk_fp8_f32 v247, v248, v249
	v_cvt_pk_fp8_f32 v247, v250, v251 op_sel:[0,0,1]
	s_nop 1
	v_permlane16_swap_b32_e32 v246, v247
	global_store_dwordx2 v[0:1], v[246:247], off offset:384
.Lt8e_3_0:
	v_lshlrev_b32_e32 v168, 16, v18
	v_and_b32_e32 v169, 0xffff0000, v18
	v_lshlrev_b32_e32 v170, 16, v19
	v_and_b32_e32 v171, 0xffff0000, v19
	v_lshlrev_b32_e32 v172, 16, v20
	v_and_b32_e32 v173, 0xffff0000, v20
	v_lshlrev_b32_e32 v174, 16, v21
	v_and_b32_e32 v175, 0xffff0000, v21
	v_pk_mul_f32 v[168:169], v[4:5], v[168:169] op_sel_hi:[0,1]
	v_pk_mul_f32 v[170:171], v[4:5], v[170:171] op_sel_hi:[0,1]
	v_pk_fma_f32 v[60:61], v[184:185], v[60:61], v[168:169] op_sel_hi:[0,1,1]
	v_pk_fma_f32 v[62:63], v[184:185], v[62:63], v[170:171] op_sel_hi:[0,1,1]
	v_pk_mul_f32 v[60:61], v[60:61], v[172:173]
	v_pk_mul_f32 v[62:63], v[62:63], v[174:175]
	v_cvt_pk_bf16_f32 v240, v60, v61
	v_cvt_pk_bf16_f32 v241, v62, v63
	v_lshlrev_b32_e32 v168, 16, v22
	v_and_b32_e32 v169, 0xffff0000, v22
	v_lshlrev_b32_e32 v170, 16, v23
	v_and_b32_e32 v171, 0xffff0000, v23
	v_lshlrev_b32_e32 v172, 16, v24
	v_and_b32_e32 v173, 0xffff0000, v24
	v_lshlrev_b32_e32 v174, 16, v25
	v_and_b32_e32 v175, 0xffff0000, v25
	v_pk_mul_f32 v[168:169], v[4:5], v[168:169] op_sel_hi:[0,1]
	v_pk_mul_f32 v[170:171], v[4:5], v[170:171] op_sel_hi:[0,1]
	v_pk_fma_f32 v[56:57], v[184:185], v[56:57], v[168:169] op_sel_hi:[0,1,1]
	v_pk_fma_f32 v[58:59], v[184:185], v[58:59], v[170:171] op_sel_hi:[0,1,1]
	v_pk_mul_f32 v[56:57], v[56:57], v[172:173]
	v_pk_mul_f32 v[58:59], v[58:59], v[174:175]
	v_cvt_pk_bf16_f32 v242, v56, v57
	v_cvt_pk_bf16_f32 v243, v58, v59
	s_nop 1
	v_permlane16_swap_b32_e32 v240, v242
	v_permlane16_swap_b32_e32 v241, v243
	global_store_dwordx4 v[2:3], v[240:243], off offset:832
	s_cbranch_vccz .Lt8e_3_1
	v_med3_f32 v248, v60, s77, v252
	v_med3_f32 v249, v61, s77, v252
	v_med3_f32 v250, v62, s77, v252
	v_med3_f32 v251, v63, s77, v252
	v_mov_b32_e32 v246, v245
	v_cvt_pk_fp8_f32 v246, v248, v249
	v_cvt_pk_fp8_f32 v246, v250, v251 op_sel:[0,0,1]
	v_med3_f32 v248, v56, s77, v252
	v_med3_f32 v249, v57, s77, v252
	v_med3_f32 v250, v58, s77, v252
	v_med3_f32 v251, v59, s77, v252
	v_mov_b32_e32 v247, v245
	v_cvt_pk_fp8_f32 v247, v248, v249
	v_cvt_pk_fp8_f32 v247, v250, v251 op_sel:[0,0,1]
	s_nop 1
	v_permlane16_swap_b32_e32 v246, v247
	global_store_dwordx2 v[0:1], v[246:247], off offset:416
.Lt8e_3_1:
	v_lshlrev_b32_e32 v168, 16, v26
	v_and_b32_e32 v169, 0xffff0000, v26
	v_lshlrev_b32_e32 v170, 16, v27
	v_and_b32_e32 v171, 0xffff0000, v27
	v_lshlrev_b32_e32 v172, 16, v28
	v_and_b32_e32 v173, 0xffff0000, v28
	v_lshlrev_b32_e32 v174, 16, v29
	v_and_b32_e32 v175, 0xffff0000, v29
	v_pk_mul_f32 v[168:169], v[4:5], v[168:169] op_sel_hi:[0,1]
	v_pk_mul_f32 v[170:171], v[4:5], v[170:171] op_sel_hi:[0,1]
	v_pk_fma_f32 v[52:53], v[184:185], v[52:53], v[168:169] op_sel_hi:[0,1,1]
	v_pk_fma_f32 v[54:55], v[184:185], v[54:55], v[170:171] op_sel_hi:[0,1,1]
	v_pk_mul_f32 v[52:53], v[52:53], v[172:173]
	v_pk_mul_f32 v[54:55], v[54:55], v[174:175]
	v_cvt_pk_bf16_f32 v240, v52, v53
	v_cvt_pk_bf16_f32 v241, v54, v55
	v_lshlrev_b32_e32 v168, 16, v30
	v_and_b32_e32 v169, 0xffff0000, v30
	v_lshlrev_b32_e32 v170, 16, v31
	v_and_b32_e32 v171, 0xffff0000, v31
	v_lshlrev_b32_e32 v172, 16, v32
	v_and_b32_e32 v173, 0xffff0000, v32
	v_lshlrev_b32_e32 v174, 16, v33
	v_and_b32_e32 v175, 0xffff0000, v33
	v_pk_mul_f32 v[168:169], v[4:5], v[168:169] op_sel_hi:[0,1]
	v_pk_mul_f32 v[170:171], v[4:5], v[170:171] op_sel_hi:[0,1]
	v_pk_fma_f32 v[48:49], v[184:185], v[48:49], v[168:169] op_sel_hi:[0,1,1]
	v_pk_fma_f32 v[50:51], v[184:185], v[50:51], v[170:171] op_sel_hi:[0,1,1]
	v_pk_mul_f32 v[48:49], v[48:49], v[172:173]
	v_pk_mul_f32 v[50:51], v[50:51], v[174:175]
	v_cvt_pk_bf16_f32 v242, v48, v49
	v_cvt_pk_bf16_f32 v243, v50, v51
	s_nop 1
	v_permlane16_swap_b32_e32 v240, v242
	v_permlane16_swap_b32_e32 v241, v243
	global_store_dwordx4 v[2:3], v[240:243], off offset:896
	s_cbranch_vccz .Lt8e_3_2
	v_med3_f32 v248, v52, s77, v252
	v_med3_f32 v249, v53, s77, v252
	v_med3_f32 v250, v54, s77, v252
	v_med3_f32 v251, v55, s77, v252
	v_mov_b32_e32 v246, v245
	v_cvt_pk_fp8_f32 v246, v248, v249
	v_cvt_pk_fp8_f32 v246, v250, v251 op_sel:[0,0,1]
	v_med3_f32 v248, v48, s77, v252
	v_med3_f32 v249, v49, s77, v252
	v_med3_f32 v250, v50, s77, v252
	v_med3_f32 v251, v51, s77, v252
	v_mov_b32_e32 v247, v245
	v_cvt_pk_fp8_f32 v247, v248, v249
	v_cvt_pk_fp8_f32 v247, v250, v251 op_sel:[0,0,1]
	s_nop 1
	v_permlane16_swap_b32_e32 v246, v247
	global_store_dwordx2 v[0:1], v[246:247], off offset:448
.Lt8e_3_2:
	v_lshlrev_b32_e32 v168, 16, v34
	v_and_b32_e32 v169, 0xffff0000, v34
	v_lshlrev_b32_e32 v170, 16, v35
	v_and_b32_e32 v171, 0xffff0000, v35
	v_lshlrev_b32_e32 v172, 16, v36
	v_and_b32_e32 v173, 0xffff0000, v36
	v_lshlrev_b32_e32 v174, 16, v37
	v_and_b32_e32 v175, 0xffff0000, v37
	v_pk_mul_f32 v[168:169], v[4:5], v[168:169] op_sel_hi:[0,1]
	v_pk_mul_f32 v[170:171], v[4:5], v[170:171] op_sel_hi:[0,1]
	v_pk_fma_f32 v[44:45], v[184:185], v[44:45], v[168:169] op_sel_hi:[0,1,1]
	v_pk_fma_f32 v[46:47], v[184:185], v[46:47], v[170:171] op_sel_hi:[0,1,1]
	v_pk_mul_f32 v[44:45], v[44:45], v[172:173]
	v_pk_mul_f32 v[46:47], v[46:47], v[174:175]
	v_cvt_pk_bf16_f32 v240, v44, v45
	v_cvt_pk_bf16_f32 v241, v46, v47
	v_lshlrev_b32_e32 v168, 16, v236
	v_and_b32_e32 v169, 0xffff0000, v236
	v_lshlrev_b32_e32 v170, 16, v237
	v_and_b32_e32 v171, 0xffff0000, v237
	v_lshlrev_b32_e32 v172, 16, v238
	v_and_b32_e32 v173, 0xffff0000, v238
	v_lshlrev_b32_e32 v174, 16, v239
	v_and_b32_e32 v175, 0xffff0000, v239
	v_pk_mul_f32 v[168:169], v[4:5], v[168:169] op_sel_hi:[0,1]
	v_pk_mul_f32 v[170:171], v[4:5], v[170:171] op_sel_hi:[0,1]
	v_pk_fma_f32 v[40:41], v[184:185], v[40:41], v[168:169] op_sel_hi:[0,1,1]
	v_pk_fma_f32 v[42:43], v[184:185], v[42:43], v[170:171] op_sel_hi:[0,1,1]
	v_pk_mul_f32 v[40:41], v[40:41], v[172:173]
	v_pk_mul_f32 v[42:43], v[42:43], v[174:175]
	v_cvt_pk_bf16_f32 v242, v40, v41
	v_cvt_pk_bf16_f32 v243, v42, v43
	s_nop 1
	v_permlane16_swap_b32_e32 v240, v242
	v_permlane16_swap_b32_e32 v241, v243
	global_store_dwordx4 v[2:3], v[240:243], off offset:960
	s_cbranch_vccz .Lt8e_3_3
	v_med3_f32 v248, v44, s77, v252
	v_med3_f32 v249, v45, s77, v252
	v_med3_f32 v250, v46, s77, v252
	v_med3_f32 v251, v47, s77, v252
	v_mov_b32_e32 v246, v245
	v_cvt_pk_fp8_f32 v246, v248, v249
	v_cvt_pk_fp8_f32 v246, v250, v251 op_sel:[0,0,1]
	v_med3_f32 v248, v40, s77, v252
	v_med3_f32 v249, v41, s77, v252
	v_med3_f32 v250, v42, s77, v252
	v_med3_f32 v251, v43, s77, v252
	v_mov_b32_e32 v247, v245
	v_cvt_pk_fp8_f32 v247, v248, v249
	v_cvt_pk_fp8_f32 v247, v250, v251 op_sel:[0,0,1]
	s_nop 1
	v_permlane16_swap_b32_e32 v246, v247
	global_store_dwordx2 v[0:1], v[246:247], off offset:480
.Lt8e_3_3:
	s_branch .LBB0_437
